# v9
# speedup vs baseline: 1.0183x; 1.0093x over previous
_Z7gemm_tnILi128ELi144ELi4ELi3ELi4ELi7ELi1EEvPKDF16_S1_PKfPfPDF16_iiiiiS3_S3_S4_:
	s_mov_b32 s12, 0x800
	s_mov_b32 s13, 0x900
	s_mov_b32 s14, 0x300
	s_mov_b32 s15, 16
	s_load_dwordx2 s[16:17], s[0:1], 0x0
	s_ashr_i32 s7, s2, 31
	s_lshr_b32 s7, s7, 29
	s_add_i32 s9, s2, s7
	s_ashr_i32 s30, s12, 31
	s_mul_hi_i32 s3, s13, 0x38e38e39
	s_lshr_b32 s4, s30, 25
	s_add_i32 s4, s12, s4
	s_lshr_b32 s5, s3, 31
	s_ashr_i32 s3, s3, 5
	s_ashr_i32 s4, s4, 7
	s_add_i32 s5, s3, s5
	s_mul_i32 s5, s5, s4
	s_ashr_i32 s3, s5, 31
	s_lshr_b32 s3, s3, 29
	s_add_i32 s6, s5, s3
	s_ashr_i32 s3, s6, 3
	s_and_b32 s6, s6, -8
	s_and_b32 s7, s9, -8
	s_sub_i32 s6, s5, s6
	s_sub_i32 s7, s2, s7
	s_add_i32 s8, s3, 1
	s_cmp_ge_i32 s7, s6
	s_cbranch_scc0 .LBB6_2
	s_mul_i32 s2, s8, s6
	s_sub_i32 s6, s7, s6
	s_mul_i32 s3, s6, s3
	s_add_i32 s6, s3, s2
	s_load_dwordx2 s[20:21], s[0:1], 0x8
	s_ashr_i32 s2, s9, 3
	s_cbranch_execz .LBB6_3
	s_branch .LBB6_4

.LBB6_4:
	s_abs_i32 s3, s5
	v_cvt_f32_u32_e32 v1, s3
	s_sub_i32 s8, 0, s3
	s_add_i32 s2, s6, s2
	s_abs_i32 s7, s2
	v_rcp_iflag_f32_e32 v1, v1
	s_xor_b32 s6, s2, s5
	s_ashr_i32 s6, s6, 31
	s_mov_b32 s23, 0x20000
	v_mul_f32_e32 v1, 0x4f7ffffe, v1
	v_cvt_u32_f32_e32 v1, v1
	s_mov_b32 s19, s23
	s_mul_i32 s25, s14, 0x60
	v_readfirstlane_b32 s9, v1
	s_mul_i32 s8, s8, s9
	s_mul_hi_u32 s8, s9, s8
	s_add_i32 s9, s9, s8
	s_mul_hi_u32 s8, s7, s9
	s_mul_i32 s9, s8, s3
	s_sub_i32 s7, s7, s9
	s_add_i32 s10, s8, 1
	s_sub_i32 s9, s7, s3
	s_cmp_ge_u32 s7, s3
	s_cselect_b32 s8, s10, s8
	s_cselect_b32 s7, s9, s7
	s_add_i32 s9, s8, 1
	s_cmp_ge_u32 s7, s3
	s_cselect_b32 s3, s9, s8
	s_abs_i32 s7, s4
	v_cvt_f32_u32_e32 v1, s7
	s_xor_b32 s3, s3, s6
	s_sub_i32 s8, 0, s7
	s_sub_i32 s3, s3, s6
	v_rcp_iflag_f32_e32 v1, v1
	s_mul_i32 s5, s3, s5
	s_sub_i32 s31, s2, s5
	s_abs_i32 s5, s31
	v_mul_f32_e32 v1, 0x4f7ffffe, v1
	v_cvt_u32_f32_e32 v1, v1
	s_xor_b32 s2, s31, s4
	s_ashr_i32 s2, s2, 31
	v_readfirstlane_b32 s6, v1
	s_mul_i32 s8, s8, s6
	s_mul_hi_u32 s8, s6, s8
	s_add_i32 s6, s6, s8
	s_mul_hi_u32 s6, s5, s6
	s_mul_i32 s8, s6, s7
	s_sub_i32 s5, s5, s8
	s_add_i32 s9, s6, 1
	s_sub_i32 s8, s5, s7
	s_cmp_ge_u32 s5, s7
	s_cselect_b32 s6, s9, s6
	s_cselect_b32 s5, s8, s5
	s_add_i32 s8, s6, 1
	s_cmp_ge_u32 s5, s7
	s_cselect_b32 s5, s8, s6
	s_xor_b32 s5, s5, s2
	s_sub_i32 s2, s5, s2
	s_mul_i32 s33, s2, s4
	s_sub_i32 s4, s31, s33
	s_lshl_b32 s28, s4, 7
	s_ashr_i32 s4, s14, 31
	v_lshrrev_b32_e32 v1, 3, v0
	s_lshr_b32 s4, s4, 26
	v_mul_lo_u32 v2, s14, v1
	v_xor_b32_e32 v1, v1, v0
	s_add_i32 s4, s14, s4
	v_lshlrev_b32_e32 v1, 3, v1
	s_ashr_i32 s29, s4, 6
	v_and_b32_e32 v1, 56, v1
	s_mul_i32 s3, s29, s3
	v_add_lshl_u32 v49, v2, v1, 1
	v_lshlrev_b32_e32 v1, 4, v0
	s_lshl_b32 s34, s3, 6
	v_add_u32_e32 v51, 0x1d00, v1
	s_mul_i32 s11, s28, s14
	s_mul_i32 s4, s12, s14
	s_add_i32 s6, s11, s34
	v_readfirstlane_b32 s3, v51
	v_readfirstlane_b32 s44, v51
	s_lshl_b32 s18, s4, 1
	s_waitcnt lgkmcnt(0)
	s_and_b32 s17, s17, 0xffff
	s_lshl_b32 s35, s6, 1
	s_mov_b32 m0, s3
	v_readfirstlane_b32 s3, v0
	buffer_load_dwordx4 v49, s[16:19], s35 offen lds
	s_and_b32 s3, s3, 0x3c0
	s_cmpk_lt_u32 s3, 0x100
	s_cselect_b64 s[4:5], -1, 0
	s_cmpk_gt_u32 s3, 0xff
	s_cbranch_scc1 .LBB6_6
	v_add_u32_e32 v2, 0x3000, v51
	s_add_i32 s6, s6, s25
	v_readfirstlane_b32 s7, v2
	s_lshl_b32 s6, s6, 1
	s_mov_b32 m0, s7
	s_nop 0
	buffer_load_dwordx4 v49, s[16:19], s6 offen lds

.LBB6_41:
	s_or_b64 exec, exec, s[0:1]
	v_lshlrev_b32_e32 v0, 3, v55
	v_lshl_or_b32 v0, v56, 8, v0
	v_add_u32_e32 v0, 0x1800, v0
	s_waitcnt lgkmcnt(0)
	s_barrier
	ds_read2_b64 v[38:41], v0 offset0:32 offset1:48
	v_or_b32_e32 v0, v1, v54
	v_lshl_add_u32 v1, v56, 5, s28
	v_or_b32_e32 v81, v1, v55
	v_lshlrev_b32_e32 v80, 2, v0
	v_mad_i64_i32 v[42:43], s[0:1], v81, s13, 0
	v_lshl_add_u64 v[74:75], v[42:43], 1, s[24:25]
	ds_read_b128 v[42:45], v80 offset:4096
	ds_read_b128 v[46:49], v80 offset:4672
	ds_read_b128 v[50:53], v80 offset:5248
	ds_read_b128 v[54:57], v80 offset:5824
	ds_read_b128 v[58:61], v80 offset:4160
	ds_read_b128 v[62:65], v80 offset:4224
	s_waitcnt lgkmcnt(4)
	v_pk_add_f32 v[76:77], v[42:43], v[46:47]
	v_pk_add_f32 v[78:79], v[44:45], v[48:49]
	s_waitcnt lgkmcnt(2)
	v_pk_add_f32 v[54:55], v[50:51], v[54:55]
	v_pk_fma_f32 v[34:35], v[38:39], v[76:77], v[34:35] op_sel_hi:[0,1,1] neg_lo:[1,0,0] neg_hi:[1,0,0]
	v_pk_fma_f32 v[34:35], v[38:39], v[34:35], v[54:55] op_sel:[1,0,0]
	v_pk_add_f32 v[56:57], v[52:53], v[56:57]
	v_pk_add_f32 v[34:35], v[10:11], v[34:35]
	ds_read_b128 v[66:69], v80 offset:5312
	ds_read_b128 v[70:73], v80 offset:5376
	v_cvt_pk_f16_f32 v88, v34, v35
	v_pk_fma_f32 v[34:35], v[38:39], v[78:79], v[36:37] op_sel_hi:[0,1,1] neg_lo:[1,0,0] neg_hi:[1,0,0]
	v_pk_fma_f32 v[34:35], v[38:39], v[34:35], v[56:57] op_sel:[1,0,0]
	v_add_u32_e32 v0, s10, v0
	v_pk_add_f32 v[34:35], v[12:13], v[34:35]
	ds_read_b128 v[42:45], v80 offset:5888
	ds_read_b128 v[50:53], v80 offset:5952
	v_cvt_pk_f16_f32 v89, v34, v35
	ds_read_b128 v[34:37], v80 offset:4736
	v_ashrrev_i32_e32 v1, 31, v0
	v_lshlrev_b64 v[0:1], 1, v[0:1]
	v_lshl_add_u64 v[74:75], v[74:75], 0, v[0:1]
	v_mbcnt_lo_u32_b32 v94, -1, 0
	v_mbcnt_hi_u32_b32 v94, -1, v94
	v_and_b32_e32 v94, 16, v94
	v_lshrrev_b32_e32 v95, 1, v94
	v_add_u32_e32 v94, v94, v95
	v_mov_b32_e32 v95, 0
	ds_read_b128 v[46:49], v80 offset:4800
	s_waitcnt lgkmcnt(1)
	v_pk_add_f32 v[34:35], v[58:59], v[34:35]
	v_pk_add_f32 v[36:37], v[60:61], v[36:37]
	v_pk_add_f32 v[42:43], v[66:67], v[42:43]
	v_pk_fma_f32 v[30:31], v[38:39], v[34:35], v[30:31] op_sel_hi:[0,1,1] neg_lo:[1,0,0] neg_hi:[1,0,0]
	v_pk_add_f32 v[44:45], v[68:69], v[44:45]
	v_pk_fma_f32 v[32:33], v[38:39], v[36:37], v[32:33] op_sel_hi:[0,1,1] neg_lo:[1,0,0] neg_hi:[1,0,0]
	v_pk_fma_f32 v[30:31], v[38:39], v[30:31], v[42:43] op_sel:[1,0,0]
	v_pk_fma_f32 v[32:33], v[38:39], v[32:33], v[44:45] op_sel:[1,0,0]
	v_pk_add_f32 v[30:31], v[6:7], v[30:31]
	v_pk_add_f32 v[32:33], v[8:9], v[32:33]
	v_cvt_pk_f16_f32 v90, v30, v31
	v_cvt_pk_f16_f32 v91, v32, v33
	v_lshl_add_u64 v[92:93], v[74:75], 0, v[94:95]
	s_nop 1
	v_permlane16_swap_b32 v88, v90
	v_permlane16_swap_b32 v89, v91
	global_store_dwordx4 v[92:93], v[88:91], off
	s_waitcnt lgkmcnt(0)
	v_pk_add_f32 v[30:31], v[62:63], v[46:47]
	v_pk_add_f32 v[46:47], v[64:65], v[48:49]
	v_pk_add_f32 v[32:33], v[70:71], v[50:51]
	v_pk_fma_f32 v[26:27], v[38:39], v[30:31], v[26:27] op_sel_hi:[0,1,1] neg_lo:[1,0,0] neg_hi:[1,0,0]
	v_pk_add_f32 v[48:49], v[72:73], v[52:53]
	v_pk_fma_f32 v[28:29], v[38:39], v[46:47], v[28:29] op_sel_hi:[0,1,1] neg_lo:[1,0,0] neg_hi:[1,0,0]
	v_pk_fma_f32 v[26:27], v[38:39], v[26:27], v[32:33] op_sel:[1,0,0]
	v_pk_fma_f32 v[28:29], v[38:39], v[28:29], v[48:49] op_sel:[1,0,0]
	v_pk_add_f32 v[26:27], v[2:3], v[26:27]
	v_pk_add_f32 v[28:29], v[4:5], v[28:29]
	v_pk_fma_f32 v[22:23], v[40:41], v[76:77], v[22:23] op_sel_hi:[0,1,1] neg_lo:[1,0,0] neg_hi:[1,0,0]
	v_cvt_pk_f16_f32 v100, v26, v27
	v_cvt_pk_f16_f32 v101, v28, v29
	v_pk_fma_f32 v[22:23], v[40:41], v[22:23], v[54:55] op_sel:[1,0,0]
	v_or_b32_e32 v26, 16, v81
	v_pk_add_f32 v[10:11], v[10:11], v[22:23]
	v_pk_fma_f32 v[22:23], v[40:41], v[78:79], v[24:25] op_sel_hi:[0,1,1] neg_lo:[1,0,0] neg_hi:[1,0,0]
	v_mad_i64_i32 v[26:27], s[0:1], v26, s13, 0
	v_pk_fma_f32 v[22:23], v[40:41], v[22:23], v[56:57] op_sel:[1,0,0]
	v_lshl_add_u64 v[26:27], v[26:27], 1, s[24:25]
	v_pk_add_f32 v[12:13], v[12:13], v[22:23]
	v_cvt_pk_f16_f32 v96, v10, v11
	v_cvt_pk_f16_f32 v97, v12, v13
	v_lshl_add_u64 v[0:1], v[26:27], 0, v[0:1]
	v_pk_fma_f32 v[10:11], v[40:41], v[34:35], v[18:19] op_sel_hi:[0,1,1] neg_lo:[1,0,0] neg_hi:[1,0,0]
	v_pk_fma_f32 v[10:11], v[40:41], v[10:11], v[42:43] op_sel:[1,0,0]
	s_nop 0
	v_pk_add_f32 v[6:7], v[6:7], v[10:11]
	v_pk_fma_f32 v[10:11], v[40:41], v[36:37], v[20:21] op_sel_hi:[0,1,1] neg_lo:[1,0,0] neg_hi:[1,0,0]
	v_pk_fma_f32 v[10:11], v[40:41], v[10:11], v[44:45] op_sel:[1,0,0]
	v_cvt_pk_f16_f32 v98, v6, v7
	v_pk_add_f32 v[8:9], v[8:9], v[10:11]
	s_nop 0
	v_cvt_pk_f16_f32 v99, v8, v9
	v_lshl_add_u64 v[92:93], v[0:1], 0, v[94:95]
	s_nop 1
	v_permlane16_swap_b32 v96, v98
	v_permlane16_swap_b32 v97, v99
	global_store_dwordx4 v[92:93], v[96:99], off
	v_pk_fma_f32 v[6:7], v[40:41], v[30:31], v[14:15] op_sel_hi:[0,1,1] neg_lo:[1,0,0] neg_hi:[1,0,0]
	v_pk_fma_f32 v[6:7], v[40:41], v[6:7], v[32:33] op_sel:[1,0,0]
	s_nop 0
	v_pk_add_f32 v[2:3], v[2:3], v[6:7]
	v_pk_fma_f32 v[6:7], v[40:41], v[46:47], v[16:17] op_sel_hi:[0,1,1] neg_lo:[1,0,0] neg_hi:[1,0,0]
	v_pk_fma_f32 v[6:7], v[40:41], v[6:7], v[48:49] op_sel:[1,0,0]
	v_cvt_pk_f16_f32 v102, v2, v3
	v_pk_add_f32 v[4:5], v[4:5], v[6:7]
	s_nop 0
	v_cvt_pk_f16_f32 v103, v4, v5
	v_bfe_u32 v95, v94, 3, 1
	v_mul_u32_u24_e32 v94, 0x11ff8, v95
	v_add_u32_e32 v94, 0xfffee040, v94
	v_add_u32_e32 v95, -1, v95
	v_lshl_add_u64 v[92:93], v[0:1], 0, v[94:95]
	v_permlane16_swap_b32 v100, v102
	v_permlane16_swap_b32 v101, v103
	global_store_dwordx4 v[92:93], v[100:103], off
	s_endpgm
	.p2align	8

	.amdhsa_kernel _Z7gemm_tnILi128ELi144ELi4ELi3ELi4ELi7ELi1EEvPKDF16_S1_PKfPfPDF16_iiiiiS3_S3_S4_
		.amdhsa_group_segment_fixed_size 7424
		.amdhsa_private_segment_fixed_size 0
		.amdhsa_kernarg_size 88
		.amdhsa_user_sgpr_count 2
		.amdhsa_user_sgpr_dispatch_ptr 0
		.amdhsa_user_sgpr_queue_ptr 0
		.amdhsa_user_sgpr_kernarg_segment_ptr 1
		.amdhsa_user_sgpr_dispatch_id 0
		.amdhsa_user_sgpr_kernarg_preload_length 0
		.amdhsa_user_sgpr_kernarg_preload_offset 0
		.amdhsa_user_sgpr_private_segment_size 0
		.amdhsa_uses_dynamic_stack 0
		.amdhsa_enable_private_segment 0
		.amdhsa_system_sgpr_workgroup_id_x 1
		.amdhsa_system_sgpr_workgroup_id_y 0
		.amdhsa_system_sgpr_workgroup_id_z 0
		.amdhsa_system_sgpr_workgroup_info 0
		.amdhsa_system_vgpr_workitem_id 0
		.amdhsa_next_free_vgpr 104
		.amdhsa_next_free_sgpr 91
		.amdhsa_accum_offset 104
		.amdhsa_reserve_vcc 1
		.amdhsa_float_round_mode_32 0
		.amdhsa_float_round_mode_16_64 0
		.amdhsa_float_denorm_mode_32 3
		.amdhsa_float_denorm_mode_16_64 3
		.amdhsa_dx10_clamp 1
		.amdhsa_ieee_mode 1
		.amdhsa_fp16_overflow 0
		.amdhsa_tg_split 0
		.amdhsa_exception_fp_ieee_invalid_op 0
		.amdhsa_exception_fp_denorm_src 0
		.amdhsa_exception_fp_ieee_div_zero 0
		.amdhsa_exception_fp_ieee_overflow 0
		.amdhsa_exception_fp_ieee_underflow 0
		.amdhsa_exception_fp_ieee_inexact 0
		.amdhsa_exception_int_div_zero 0
	.end_amdhsa_kernel

.LBB9_7:
	s_waitcnt vmcnt(30)
	s_add_i32 s19, s9, 7
	s_cmp_ge_i32 s19, s24
	s_barrier
	s_cbranch_scc1 .LBB9_6
	s_and_b32 s19, s19, 7
	s_mulk_i32 s19, 0x5000
	s_add_i32 s27, s40, s19
	s_add_i32 s41, s25, s22
	s_add_i32 s42, s10, s22
	s_add_i32 s43, s26, s22
	s_add_i32 s44, s23, s22
	s_add_i32 s45, s21, s22
	s_mov_b32 m0, s27
	s_and_b32 s28, s9, 7
	s_mulk_i32 s28, 0x5000
	buffer_load_dwordx4 v51, s[12:15], s41 offen lds
	v_add_u32_e32 v55, s28, v50
	v_lshlrev_b32_e32 v60, 1, v53
	v_add_u32_e32 v88, s28, v0
	v_add_u32_e32 v61, v55, v60
	v_add_u32_e32 v60, v88, v60
	ds_read_b128 v[56:59], v61 offset:8192
	ds_read_b128 v[72:75], v60
	ds_read_b128 v[76:79], v61 offset:10240
	ds_read_b128 v[80:83], v60 offset:2048
	ds_read_b128 v[84:87], v61 offset:12288
	v_lshlrev_b32_e32 v60, 1, v54
	v_add_u32_e32 v61, v88, v60
	v_add_u32_e32 v55, v55, v60
	s_add_i32 s27, s27, 0x1000
	s_add_i32 s9, s9, 1
	s_addk_i32 s22, 0x80
	s_mov_b32 m0, s27
	s_waitcnt lgkmcnt(3)
	v_mfma_f32_16x16x32_f16 a[0:3], v[56:59], v[72:75], a[0:3]
	ds_read_b128 v[88:91], v61
	buffer_load_dwordx4 v51, s[12:15], s42 offen lds
	s_add_i32 s27, s27, 0x1000
	s_waitcnt lgkmcnt(3)
	v_mfma_f32_16x16x32_f16 a[4:7], v[76:79], v[72:75], a[4:7]
	s_waitcnt lgkmcnt(1)
	v_mfma_f32_16x16x32_f16 a[8:11], v[84:87], v[72:75], a[8:11]
	ds_read_b128 v[72:75], v55 offset:10240
	s_mov_b32 m0, s27
	s_mov_b32 s19, s15
	v_mfma_f32_16x16x32_f16 a[12:15], v[56:59], v[80:83], a[12:15]
	ds_read_b128 v[56:59], v55 offset:8192
	buffer_load_dwordx4 v51, s[16:19], s43 offen lds
	s_add_i32 s27, s27, 0x1000
	v_mfma_f32_16x16x32_f16 a[16:19], v[76:79], v[80:83], a[16:19]
	ds_read_b128 v[76:79], v55 offset:12288
	s_mov_b32 m0, s27
	v_mfma_f32_16x16x32_f16 a[20:23], v[84:87], v[80:83], a[20:23]
	ds_read_b128 v[80:83], v61 offset:2048
	buffer_load_dwordx4 v51, s[16:19], s44 offen lds
	s_add_i32 s27, s27, 0x1000
	s_waitcnt lgkmcnt(2)
	v_mfma_f32_16x16x32_f16 a[0:3], v[56:59], v[88:91], a[0:3]
	s_mov_b32 m0, s27
	v_mfma_f32_16x16x32_f16 a[4:7], v[72:75], v[88:91], a[4:7]
	buffer_load_dwordx4 v51, s[16:19], s45 offen lds
	s_waitcnt lgkmcnt(1)
	v_mfma_f32_16x16x32_f16 a[8:11], v[76:79], v[88:91], a[8:11]
	s_waitcnt lgkmcnt(0)
	v_mfma_f32_16x16x32_f16 a[12:15], v[56:59], v[80:83], a[12:15]
	v_mfma_f32_16x16x32_f16 a[16:19], v[72:75], v[80:83], a[16:19]
	s_cmp_lg_u32 s20, s9
	v_mfma_f32_16x16x32_f16 a[20:23], v[76:79], v[80:83], a[20:23]
	s_cbranch_scc1 .LBB9_7
	s_branch .LBB9_9

amdhsa.kernels:
  - .agpr_count:     0
    .args:
      - .actual_access:  read_only
        .address_space:  global
        .offset:         0
        .size:           8
        .value_kind:     global_buffer
      - .actual_access:  write_only
        .address_space:  global
        .offset:         8
        .size:           8
        .value_kind:     global_buffer
      - .offset:         16
        .size:           4
        .value_kind:     by_value
      - .offset:         20
        .size:           4
        .value_kind:     by_value
      - .offset:         24
        .size:           4
        .value_kind:     by_value
    .group_segment_fixed_size: 17408
    .kernarg_segment_align: 8
    .kernarg_segment_size: 28
    .language:       OpenCL C
    .language_version:
      - 2
      - 0
    .max_flat_workgroup_size: 256
    .name:           _Z13conv_w_kernelPKfPDF16_iii
    .private_segment_fixed_size: 0
    .sgpr_count:     23
    .sgpr_spill_count: 0
    .symbol:         _Z13conv_w_kernelPKfPDF16_iii.kd
    .uniform_work_group_size: 1
    .uses_dynamic_stack: false
    .vgpr_count:     52
    .vgpr_spill_count: 0
    .wavefront_size: 64
  - .agpr_count:     0
    .args:
      - .offset:         0
        .size:           264
        .value_kind:     by_value
    .group_segment_fixed_size: 17408
    .kernarg_segment_align: 8
    .kernarg_segment_size: 264
    .language:       OpenCL C
    .language_version:
      - 2
      - 0
    .max_flat_workgroup_size: 256
    .name:           _Z15conv_all_kernel7ConvJob
    .private_segment_fixed_size: 0
    .sgpr_count:     78
    .sgpr_spill_count: 0
    .symbol:         _Z15conv_all_kernel7ConvJob.kd
    .uniform_work_group_size: 1
    .uses_dynamic_stack: false
    .vgpr_count:     62
    .vgpr_spill_count: 0
    .wavefront_size: 64
  - .agpr_count:     0
    .args:
      - .actual_access:  read_only
        .address_space:  global
        .offset:         0
        .size:           8
        .value_kind:     global_buffer
      - .actual_access:  read_only
        .address_space:  global
        .offset:         8
        .size:           8
        .value_kind:     global_buffer
      - .actual_access:  read_only
        .address_space:  global
        .offset:         16
        .size:           8
        .value_kind:     global_buffer
      - .actual_access:  read_only
        .address_space:  global
        .offset:         24
        .size:           8
        .value_kind:     global_buffer
      - .actual_access:  read_only
        .address_space:  global
        .offset:         32
        .size:           8
        .value_kind:     global_buffer
      - .actual_access:  write_only
        .address_space:  global
        .offset:         40
        .size:           8
        .value_kind:     global_buffer
      - .actual_access:  write_only
        .address_space:  global
        .offset:         48
        .size:           8
        .value_kind:     global_buffer
      - .offset:         56
        .size:           264
        .value_kind:     by_value
    .group_segment_fixed_size: 17408
    .kernarg_segment_align: 8
    .kernarg_segment_size: 320
    .language:       OpenCL C
    .language_version:
      - 2
      - 0
    .max_flat_workgroup_size: 256
    .name:           _Z15embed_ln_kernelPKiPKfS2_S2_S2_PfPDF16_7ConvJob
    .private_segment_fixed_size: 0
    .sgpr_count:     74
    .sgpr_spill_count: 0
    .symbol:         _Z15embed_ln_kernelPKiPKfS2_S2_S2_PfPDF16_7ConvJob.kd
    .uniform_work_group_size: 1
    .uses_dynamic_stack: false
    .vgpr_count:     62
    .vgpr_spill_count: 0
    .wavefront_size: 64
  - .agpr_count:     0
    .args:
      - .actual_access:  read_only
        .address_space:  global
        .offset:         0
        .size:           8
        .value_kind:     global_buffer
      - .actual_access:  read_only
        .address_space:  global
        .offset:         8
        .size:           8
        .value_kind:     global_buffer
      - .actual_access:  read_only
        .address_space:  global
        .offset:         16
        .size:           8
        .value_kind:     global_buffer
      - .actual_access:  write_only
        .address_space:  global
        .offset:         24
        .size:           8
        .value_kind:     global_buffer
      - .offset:         32
        .size:           264
        .value_kind:     by_value
    .group_segment_fixed_size: 17408
    .kernarg_segment_align: 8
    .kernarg_segment_size: 296
    .language:       OpenCL C
    .language_version:
      - 2
      - 0
    .max_flat_workgroup_size: 256
    .name:           _Z9ln_kernelPKfS0_S0_PDF16_7ConvJob
    .private_segment_fixed_size: 0
    .sgpr_count:     74
    .sgpr_spill_count: 0
    .symbol:         _Z9ln_kernelPKfS0_S0_PDF16_7ConvJob.kd
    .uniform_work_group_size: 1
    .uses_dynamic_stack: false
    .vgpr_count:     62
    .vgpr_spill_count: 0
    .wavefront_size: 64
  - .agpr_count:     0
    .args:
      - .actual_access:  read_only
        .address_space:  global
        .offset:         0
        .size:           8
        .value_kind:     global_buffer
      - .actual_access:  write_only
        .address_space:  global
        .offset:         8
        .size:           8
        .value_kind:     global_buffer
      - .offset:         16
        .size:           264
        .value_kind:     by_value
    .group_segment_fixed_size: 35072
    .kernarg_segment_align: 8
    .kernarg_segment_size: 280
    .language:       OpenCL C
    .language_version:
      - 2
      - 0
    .max_flat_workgroup_size: 512
    .name:           _Z18attn_rowsum_kernelPKDF16_PDF16_7ConvJob
    .private_segment_fixed_size: 0
    .sgpr_count:     74
    .sgpr_spill_count: 0
    .symbol:         _Z18attn_rowsum_kernelPKDF16_PDF16_7ConvJob.kd
    .uniform_work_group_size: 1
    .uses_dynamic_stack: false
    .vgpr_count:     72
    .vgpr_spill_count: 0
    .wavefront_size: 64
  - .agpr_count:     0
    .args:
      - .actual_access:  read_only
        .address_space:  global
        .offset:         0
        .size:           8
        .value_kind:     global_buffer
      - .actual_access:  read_only
        .address_space:  global
        .offset:         8
        .size:           8
        .value_kind:     global_buffer
      - .actual_access:  read_only
        .address_space:  global
        .offset:         16
        .size:           8
        .value_kind:     global_buffer
      - .address_space:  global
        .offset:         24
        .size:           8
        .value_kind:     global_buffer
      - .actual_access:  write_only
        .address_space:  global
        .offset:         32
        .size:           8
        .value_kind:     global_buffer
      - .offset:         40
        .size:           4
        .value_kind:     by_value
      - .offset:         44
        .size:           4
        .value_kind:     by_value
      - .offset:         48
        .size:           4
        .value_kind:     by_value
      - .offset:         52
        .size:           4
        .value_kind:     by_value
      - .offset:         56
        .size:           4
        .value_kind:     by_value
      - .actual_access:  read_only
        .address_space:  global
        .offset:         64
        .size:           8
        .value_kind:     global_buffer
      - .actual_access:  read_only
        .address_space:  global
        .offset:         72
        .size:           8
        .value_kind:     global_buffer
      - .address_space:  global
        .offset:         80
        .size:           8
        .value_kind:     global_buffer
    .group_segment_fixed_size: 0
    .kernarg_segment_align: 8
    .kernarg_segment_size: 88
    .language:       OpenCL C
    .language_version:
      - 2
      - 0
    .max_flat_workgroup_size: 768
    .name:           _Z7gemm_tnILi128ELi144ELi4ELi3ELi4ELi0ELi1EEvPKDF16_S1_PKfPfPDF16_iiiiiS3_S3_S4_
    .private_segment_fixed_size: 0
    .sgpr_count:     37
    .sgpr_spill_count: 0
    .symbol:         _Z7gemm_tnILi128ELi144ELi4ELi3ELi4ELi0ELi1EEvPKDF16_S1_PKfPfPDF16_iiiiiS3_S3_S4_.kd
    .uniform_work_group_size: 1
    .uses_dynamic_stack: false
    .vgpr_count:     68
    .vgpr_spill_count: 0
    .wavefront_size: 64
  - .agpr_count:     0
    .args:
      - .actual_access:  read_only
        .address_space:  global
        .offset:         0
        .size:           8
        .value_kind:     global_buffer
      - .actual_access:  read_only
        .address_space:  global
        .offset:         8
        .size:           8
        .value_kind:     global_buffer
      - .actual_access:  read_only
        .address_space:  global
        .offset:         16
        .size:           8
        .value_kind:     global_buffer
      - .address_space:  global
        .offset:         24
        .size:           8
        .value_kind:     global_buffer
      - .actual_access:  write_only
        .address_space:  global
        .offset:         32
        .size:           8
        .value_kind:     global_buffer
      - .offset:         40
        .size:           4
        .value_kind:     by_value
      - .offset:         44
        .size:           4
        .value_kind:     by_value
      - .offset:         48
        .size:           4
        .value_kind:     by_value
      - .offset:         52
        .size:           4
        .value_kind:     by_value
      - .offset:         56
        .size:           4
        .value_kind:     by_value
      - .actual_access:  read_only
        .address_space:  global
        .offset:         64
        .size:           8
        .value_kind:     global_buffer
      - .actual_access:  read_only
        .address_space:  global
        .offset:         72
        .size:           8
        .value_kind:     global_buffer
      - .address_space:  global
        .offset:         80
        .size:           8
        .value_kind:     global_buffer
    .group_segment_fixed_size: 7424
    .kernarg_segment_align: 8
    .kernarg_segment_size: 88
    .language:       OpenCL C
    .language_version:
      - 2
      - 0
    .max_flat_workgroup_size: 768
    .name:           _Z7gemm_tnILi128ELi144ELi4ELi3ELi4ELi7ELi1EEvPKDF16_S1_PKfPfPDF16_iiiiiS3_S3_S4_
    .private_segment_fixed_size: 0
    .sgpr_count:     46
    .sgpr_spill_count: 0
    .symbol:         _Z7gemm_tnILi128ELi144ELi4ELi3ELi4ELi7ELi1EEvPKDF16_S1_PKfPfPDF16_iiiiiS3_S3_S4_.kd
    .uniform_work_group_size: 1
    .uses_dynamic_stack: false
    .vgpr_count:     104
    .vgpr_spill_count: 0
    .wavefront_size: 64
  - .agpr_count:     24
    .args:
      - .actual_access:  read_only
        .address_space:  global
        .offset:         0
        .size:           8
        .value_kind:     global_buffer
      - .actual_access:  read_only
        .address_space:  global
        .offset:         8
        .size:           8
        .value_kind:     global_buffer
      - .actual_access:  read_only
        .address_space:  global
        .offset:         16
        .size:           8
        .value_kind:     global_buffer
      - .address_space:  global
        .offset:         24
        .size:           8
        .value_kind:     global_buffer
      - .actual_access:  read_only
        .address_space:  global
        .offset:         32
        .size:           8
        .value_kind:     global_buffer
      - .offset:         40
        .size:           4
        .value_kind:     by_value
      - .offset:         44
        .size:           4
        .value_kind:     by_value
      - .offset:         48
        .size:           4
        .value_kind:     by_value
      - .offset:         52
        .size:           4
        .value_kind:     by_value
      - .offset:         56
        .size:           4
        .value_kind:     by_value
      - .actual_access:  read_only
        .address_space:  global
        .offset:         64
        .size:           8
        .value_kind:     global_buffer
      - .actual_access:  read_only
        .address_space:  global
        .offset:         72
        .size:           8
        .value_kind:     global_buffer
      - .address_space:  global
        .offset:         80
        .size:           8
        .value_kind:     global_buffer
    .group_segment_fixed_size: 0
    .kernarg_segment_align: 8
    .kernarg_segment_size: 88
    .language:       OpenCL C
    .language_version:
      - 2
      - 0
    .max_flat_workgroup_size: 256
    .name:           _Z7gemm_tnILi64ELi96ELi2ELi2ELi8ELi2ELi1EEvPKDF16_S1_PKfPfPDF16_iiiiiS3_S3_S4_
    .private_segment_fixed_size: 0
    .sgpr_count:     46
    .sgpr_spill_count: 0
    .symbol:         _Z7gemm_tnILi64ELi96ELi2ELi2ELi8ELi2ELi1EEvPKDF16_S1_PKfPfPDF16_iiiiiS3_S3_S4_.kd
    .uniform_work_group_size: 1
    .uses_dynamic_stack: false
    .vgpr_count:     100
    .vgpr_spill_count: 0
    .wavefront_size: 64
  - .agpr_count:     0
    .args:
      - .actual_access:  read_only
        .address_space:  global
        .offset:         0
        .size:           8
        .value_kind:     global_buffer
      - .actual_access:  read_only
        .address_space:  global
        .offset:         8
        .size:           8
        .value_kind:     global_buffer
      - .actual_access:  read_only
        .address_space:  global
        .offset:         16
        .size:           8
        .value_kind:     global_buffer
      - .address_space:  global
        .offset:         24
        .size:           8
        .value_kind:     global_buffer
      - .actual_access:  write_only
        .address_space:  global
        .offset:         32
        .size:           8
        .value_kind:     global_buffer
      - .offset:         40
        .size:           4
        .value_kind:     by_value
      - .offset:         44
        .size:           4
        .value_kind:     by_value
      - .offset:         48
        .size:           4
        .value_kind:     by_value
      - .offset:         52
        .size:           4
        .value_kind:     by_value
      - .offset:         56
        .size:           4
        .value_kind:     by_value
      - .actual_access:  read_only
        .address_space:  global
        .offset:         64
        .size:           8
        .value_kind:     global_buffer
      - .actual_access:  read_only
        .address_space:  global
        .offset:         72
        .size:           8
        .value_kind:     global_buffer
      - .address_space:  global
        .offset:         80
        .size:           8
        .value_kind:     global_buffer
    .group_segment_fixed_size: 8192
    .kernarg_segment_align: 8
    .kernarg_segment_size: 88
    .language:       OpenCL C
    .language_version:
      - 2
      - 0
    .max_flat_workgroup_size: 512
    .name:           _Z7gemm_tnILi128ELi192ELi2ELi4ELi3ELi6ELi1EEvPKDF16_S1_PKfPfPDF16_iiiiiS3_S3_S4_
    .private_segment_fixed_size: 0
    .sgpr_count:     54
    .sgpr_spill_count: 0
    .symbol:         _Z7gemm_tnILi128ELi192ELi2ELi4ELi3ELi6ELi1EEvPKDF16_S1_PKfPfPDF16_iiiiiS3_S3_S4_.kd
    .uniform_work_group_size: 1
    .uses_dynamic_stack: false
    .vgpr_count:     140
    .vgpr_spill_count: 0
    .wavefront_size: 64
  - .agpr_count:     24
    .args:
      - .actual_access:  read_only
        .address_space:  global
        .offset:         0
        .size:           8
        .value_kind:     global_buffer
      - .actual_access:  read_only
        .address_space:  global
        .offset:         8
        .size:           8
        .value_kind:     global_buffer
      - .actual_access:  read_only
        .address_space:  global
        .offset:         16
        .size:           8
        .value_kind:     global_buffer
      - .address_space:  global
        .offset:         24
        .size:           8
        .value_kind:     global_buffer
      - .actual_access:  write_only
        .address_space:  global
        .offset:         32
        .size:           8
        .value_kind:     global_buffer
      - .offset:         40
        .size:           4
        .value_kind:     by_value
      - .offset:         44
        .size:           4
        .value_kind:     by_value
      - .offset:         48
        .size:           4
        .value_kind:     by_value
      - .offset:         52
        .size:           4
        .value_kind:     by_value
      - .offset:         56
        .size:           4
        .value_kind:     by_value
      - .actual_access:  read_only
        .address_space:  global
        .offset:         64
        .size:           8
        .value_kind:     global_buffer
      - .actual_access:  read_only
        .address_space:  global
        .offset:         72
        .size:           8
        .value_kind:     global_buffer
      - .address_space:  global
        .offset:         80
        .size:           8
        .value_kind:     global_buffer
    .group_segment_fixed_size: 0
    .kernarg_segment_align: 8
    .kernarg_segment_size: 88
    .language:       OpenCL C
    .language_version:
      - 2
      - 0
    .max_flat_workgroup_size: 256
    .name:           _Z7gemm_tnILi64ELi96ELi2ELi2ELi8ELi5ELi1EEvPKDF16_S1_PKfPfPDF16_iiiiiS3_S3_S4_
    .private_segment_fixed_size: 0
    .sgpr_count:     52
    .sgpr_spill_count: 0
    .symbol:         _Z7gemm_tnILi64ELi96ELi2ELi2ELi8ELi5ELi1EEvPKDF16_S1_PKfPfPDF16_iiiiiS3_S3_S4_.kd
    .uniform_work_group_size: 1
    .uses_dynamic_stack: false
    .vgpr_count:     128
    .vgpr_spill_count: 0
    .wavefront_size: 64
  - .agpr_count:     0
    .args:
      - .actual_access:  read_only
        .address_space:  global
        .offset:         0
        .size:           8
        .value_kind:     global_buffer
      - .actual_access:  read_only
        .address_space:  global
        .offset:         8
        .size:           8
        .value_kind:     global_buffer
      - .actual_access:  read_only
        .address_space:  global
        .offset:         16
        .size:           8
        .value_kind:     global_buffer
      - .address_space:  global
        .offset:         24
        .size:           8
        .value_kind:     global_buffer
      - .actual_access:  read_only
        .address_space:  global
        .offset:         32
        .size:           8
        .value_kind:     global_buffer
      - .offset:         40
        .size:           4
        .value_kind:     by_value
      - .offset:         44
        .size:           4
        .value_kind:     by_value
      - .offset:         48
        .size:           4
        .value_kind:     by_value
      - .offset:         52
        .size:           4
        .value_kind:     by_value
      - .offset:         56
        .size:           4
        .value_kind:     by_value
      - .actual_access:  read_only
        .address_space:  global
        .offset:         64
        .size:           8
        .value_kind:     global_buffer
      - .actual_access:  read_only
        .address_space:  global
        .offset:         72
        .size:           8
        .value_kind:     global_buffer
      - .address_space:  global
        .offset:         80
        .size:           8
        .value_kind:     global_buffer
    .group_segment_fixed_size: 0
    .kernarg_segment_align: 8
    .kernarg_segment_size: 88
    .language:       OpenCL C
    .language_version:
      - 2
      - 0
    .max_flat_workgroup_size: 512
    .name:           _Z7gemm_tnILi128ELi192ELi2ELi4ELi3ELi3ELi4EEvPKDF16_S1_PKfPfPDF16_iiiiiS3_S3_S4_
    .private_segment_fixed_size: 0
    .sgpr_count:     40
    .sgpr_spill_count: 0
    .symbol:         _Z7gemm_tnILi128ELi192ELi2ELi4ELi3ELi3ELi4EEvPKDF16_S1_PKfPfPDF16_iiiiiS3_S3_S4_.kd
    .uniform_work_group_size: 1
    .uses_dynamic_stack: false
    .vgpr_count:     102
    .vgpr_spill_count: 0
    .wavefront_size: 64
  - .agpr_count:     0
    .args:
      - .address_space:  global
        .offset:         0
        .size:           8
        .value_kind:     global_buffer
      - .address_space:  global
        .offset:         8
        .size:           8
        .value_kind:     global_buffer
      - .address_space:  global
        .offset:         16
        .size:           8
        .value_kind:     global_buffer
      - .offset:         24
        .size:           4
        .value_kind:     by_value
      - .offset:         28
        .size:           4
        .value_kind:     by_value
      - .offset:         32
        .size:           4
        .value_kind:     by_value
      - .offset:         36
        .size:           4
        .value_kind:     by_value
      - .offset:         40
        .size:           4
        .value_kind:     by_value
    .group_segment_fixed_size: 0
    .kernarg_segment_align: 8
    .kernarg_segment_size: 44
    .language:       OpenCL C
    .language_version:
      - 2
      - 0
    .max_flat_workgroup_size: 512
    .name:           _Z17gemm_256sq_8phaseILi0EEvPKDF16_S1_Pfiiiii
    .private_segment_fixed_size: 0
    .sgpr_count:     48
    .sgpr_spill_count: 0
    .symbol:         _Z17gemm_256sq_8phaseILi0EEvPKDF16_S1_Pfiiiii.kd
    .uniform_work_group_size: 1
    .uses_dynamic_stack: false
    .vgpr_count:     244
    .vgpr_spill_count: 0
    .wavefront_size: 64
